# v057 + in-projection GEMM: the MFMA blocks of the padding columns (tile columns 128..255 of the ninth column tile) are skipped
# speedup vs baseline: 1.0022x; 1.0022x over previous
; #define PG8_STAGE(bufoff, gbase, voff) do { _Pragma("unroll") for (int _i = 0; _i < 2; ++_i) \
;         __builtin_amdgcn_global_load_lds((const unsigned*)((const char*)(gbase) + (voff)[_i]), (LAS unsigned*)(lds + (bufoff) + ldsw + _i * 8192), 16, 0, 0); } while (0)
; #define PG8_LDA(dst, b, h) do { _Pragma("unroll") for (int m = 0; m < 4; ++m) _Pragma("unroll") for (int k = 0; k < 2; ++k) dst[m][k] = *(const LAS bf16x8*)(lds + PG8_SA(b, h) + aoff + m * 2048 + k * 1024); } while (0)
; #define PG8_LDB(dst, b, h) do { _Pragma("unroll") for (int n = 0; n < 2; ++n) _Pragma("unroll") for (int k = 0; k < 2; ++k) dst[n][k] = *(const LAS bf16x8*)(lds + PG8_SB(b, h) + boff + n * 2048 + k * 1024); } while (0)
; #define PG8_MMA(ai, bj, At, Bt_) do { __builtin_amdgcn_s_setprio(1); _Pragma("unroll") for (int m = 0; m < 4; ++m) _Pragma("unroll") for (int n = 0; n < 2; ++n) _Pragma("unroll") for (int k = 0; k < 2; ++k) \
;         acc[ai][bj][m][n] = __builtin_amdgcn_mfma_f32_16x16x32_bf16(Bt_[n][k], At[m][k], acc[ai][bj][m][n], 0, 0, 0); __builtin_amdgcn_s_setprio(0); } while (0)
; #define PG8_WAIT_L(n) asm volatile("s_waitcnt lgkmcnt(" #n ")" ::: "memory")
; #define PG8_BAR __builtin_amdgcn_s_barrier()
; #define PG8_SCHED __builtin_amdgcn_sched_barrier(0)
; template <class Epi, class Sched, bool GATHER>
; __device__ __forceinline__ void gemm_phase(LAS unsigned char* lds, const int wid, const bf16_t* A, int lda, const bf16_t* Bt, int ldb, size_t b_estride, int K, const Sched& S, const Epi& E) {
;     ...
;             PG8_LDB(B0, 0, 0); PG8_LDB(B1, 0, 1); PG8_SCHED; PG8_LDA(At, 0, 0);
;             PG8_WAIT_VR(rl); PG8_WAIT_L(0); PG8_BAR; PG8_MMA(0, 0, At, B0); PG8_MMA(0, 1, At, B1); PG8_BAR; PG8_SCHED;
;             PG8_LDA(At, 0, 1); PG8_STAGE(PG8_SB(0, 0), b2, voffB); PG8_STAGE(PG8_SB(0, 1), b2 + hstepB, voffB); PG8_STAGE_A(PG8_SA(0, 0), a2, 0, k2, g20);
;             PG8_WAIT_VR(rl); PG8_WAIT_L(0); PG8_BAR; PG8_MMA(1, 0, At, B0); PG8_MMA(1, 1, At, B1); PG8_BAR; PG8_SCHED;
;             PG8_LDB(B0, 1, 0); PG8_LDB(B1, 1, 1); PG8_SCHED; PG8_LDA(At, 1, 0); PG8_STAGE_A(PG8_SA(0, 1), a2, 1, k2, g21);
;             PG8_WAIT_VR(rl); PG8_WAIT_L(0); PG8_BAR; PG8_MMA(0, 0, At, B0); PG8_MMA(0, 1, At, B1); PG8_BAR; PG8_SCHED;
;             PG8_LDA(At, 1, 1); PG8_STAGE(PG8_SB(1, 0), b3, voffB); PG8_STAGE(PG8_SB(1, 1), b3 + hstepB, voffB); PG8_STAGE_A(PG8_SA(1, 0), a3, 0, k3, g20);
.Lwvr0:
	s_waitcnt vmcnt(24)
	s_waitcnt lgkmcnt(0)
	s_barrier
	s_setprio 1
	s_waitcnt lgkmcnt(0)
	v_mfma_f32_16x16x32_bf16 v[124:127], v[128:131], v[182:185], v[124:127]
	v_mfma_f32_16x16x32_bf16 v[120:123], v[136:139], v[182:185], v[120:123]
	v_mfma_f32_16x16x32_bf16 v[108:111], v[128:131], v[190:193], v[108:111]
	v_mfma_f32_16x16x32_bf16 v[104:107], v[136:139], v[190:193], v[104:107]
	v_mfma_f32_16x16x32_bf16 v[92:95], v[128:131], v[200:203], v[92:95]
	v_mfma_f32_16x16x32_bf16 v[88:91], v[136:139], v[200:203], v[88:91]
	v_mfma_f32_16x16x32_bf16 v[76:79], v[128:131], v[208:211], v[76:79]
	v_mfma_f32_16x16x32_bf16 v[72:75], v[136:139], v[208:211], v[72:75]
	v_mfma_f32_16x16x32_bf16 v[124:127], v[132:135], v[186:189], v[124:127]
	v_mfma_f32_16x16x32_bf16 v[120:123], v[140:143], v[186:189], v[120:123]
	v_mfma_f32_16x16x32_bf16 v[108:111], v[132:135], v[194:197], v[108:111]
	v_mfma_f32_16x16x32_bf16 v[104:107], v[140:143], v[194:197], v[104:107]
	v_mfma_f32_16x16x32_bf16 v[92:95], v[132:135], v[204:207], v[92:95]
	v_mfma_f32_16x16x32_bf16 v[88:91], v[140:143], v[204:207], v[88:91]
	v_mfma_f32_16x16x32_bf16 v[76:79], v[132:135], v[212:215], v[76:79]
	v_mfma_f32_16x16x32_bf16 v[72:75], v[140:143], v[212:215], v[72:75]
	s_setprio 0
	s_cmp_eq_u32 s14, 8
	s_cbranch_scc1 .Lmy_p2skip1
	s_setprio 1
	v_mfma_f32_16x16x32_bf16 v[116:119], v[144:147], v[182:185], v[116:119]
	v_mfma_f32_16x16x32_bf16 v[112:115], v[166:169], v[182:185], v[112:115]
	v_mfma_f32_16x16x32_bf16 v[100:103], v[144:147], v[190:193], v[100:103]
	v_mfma_f32_16x16x32_bf16 v[96:99], v[166:169], v[190:193], v[96:99]
	v_mfma_f32_16x16x32_bf16 v[84:87], v[144:147], v[200:203], v[84:87]
	v_mfma_f32_16x16x32_bf16 v[80:83], v[166:169], v[200:203], v[80:83]
	v_mfma_f32_16x16x32_bf16 v[68:71], v[144:147], v[208:211], v[68:71]
	v_mfma_f32_16x16x32_bf16 v[64:67], v[166:169], v[208:211], v[64:67]
	v_mfma_f32_16x16x32_bf16 v[116:119], v[148:151], v[186:189], v[116:119]
	v_mfma_f32_16x16x32_bf16 v[112:115], v[170:173], v[186:189], v[112:115]
	v_mfma_f32_16x16x32_bf16 v[100:103], v[148:151], v[194:197], v[100:103]
	v_mfma_f32_16x16x32_bf16 v[96:99], v[170:173], v[194:197], v[96:99]
	v_mfma_f32_16x16x32_bf16 v[84:87], v[148:151], v[204:207], v[84:87]
	v_mfma_f32_16x16x32_bf16 v[80:83], v[170:173], v[204:207], v[80:83]
	v_mfma_f32_16x16x32_bf16 v[68:71], v[148:151], v[212:215], v[68:71]
	v_mfma_f32_16x16x32_bf16 v[64:67], v[170:173], v[212:215], v[64:67]
.Lmy_p2skip1:
	s_setprio 0
	s_barrier
	s_add_i32 s96, s87, s33
	s_add_u32 s98, s70, 0x80
	s_addc_u32 s99, s71, 0
	s_mov_b32 m0, s96
	ds_read_b128 v[182:185], v177 offset:16384
	ds_read_b128 v[186:189], v177 offset:17408
	ds_read_b128 v[190:193], v177 offset:18432
	ds_read_b128 v[194:197], v177 offset:19456
	ds_read_b128 v[200:203], v177 offset:20480
	ds_read_b128 v[204:207], v177 offset:21504
	ds_read_b128 v[208:211], v177 offset:22528
	ds_read_b128 v[212:215], v177 offset:23552
	global_load_lds_dwordx4 v154, s[70:71]
	s_add_i32 m0, s96, 0x2000
	s_add_u32 s96, s70, 0x40000
	s_addc_u32 s97, s71, 0
	s_add_i32 vcc_lo, s88, s33
	global_load_lds_dwordx4 v158, s[70:71]
	s_mov_b32 m0, vcc_lo
	s_add_u32 s100, s60, 0x80
	s_addc_u32 s101, s61, 0
	global_load_lds_dwordx4 v154, s[96:97]
	s_add_i32 m0, vcc_lo, 0x2000
	s_nop 0
	global_load_lds_dwordx4 v158, s[96:97]
	s_mov_b32 m0, s15
	s_nop 0
	global_load_lds_dwordx4 v152, s[60:61]
	s_mov_b32 m0, s74
	s_nop 0
	global_load_lds_dwordx4 v156, s[60:61]
	s_cmp_lg_u32 s95, 0
	s_cbranch_scc1 .Lwvr1
	s_waitcnt vmcnt(8)
.Lwvr1:
	s_waitcnt vmcnt(24)
	s_waitcnt lgkmcnt(0)
	s_barrier
	s_setprio 1
	s_waitcnt lgkmcnt(0)
	v_mfma_f32_16x16x32_bf16 v[60:63], v[128:131], v[182:185], v[60:63]
	v_mfma_f32_16x16x32_bf16 v[56:59], v[136:139], v[182:185], v[56:59]
	v_mfma_f32_16x16x32_bf16 v[44:47], v[128:131], v[190:193], v[44:47]
	v_mfma_f32_16x16x32_bf16 v[40:43], v[136:139], v[190:193], v[40:43]
	v_mfma_f32_16x16x32_bf16 v[28:31], v[128:131], v[200:203], v[28:31]
	v_mfma_f32_16x16x32_bf16 v[24:27], v[136:139], v[200:203], v[24:27]
	v_mfma_f32_16x16x32_bf16 v[12:15], v[128:131], v[208:211], v[12:15]
	v_mfma_f32_16x16x32_bf16 v[8:11], v[136:139], v[208:211], v[8:11]
	v_mfma_f32_16x16x32_bf16 v[60:63], v[132:135], v[186:189], v[60:63]
	v_mfma_f32_16x16x32_bf16 v[56:59], v[140:143], v[186:189], v[56:59]
	v_mfma_f32_16x16x32_bf16 v[44:47], v[132:135], v[194:197], v[44:47]
	v_mfma_f32_16x16x32_bf16 v[40:43], v[140:143], v[194:197], v[40:43]
	v_mfma_f32_16x16x32_bf16 v[28:31], v[132:135], v[204:207], v[28:31]
	v_mfma_f32_16x16x32_bf16 v[24:27], v[140:143], v[204:207], v[24:27]
	v_mfma_f32_16x16x32_bf16 v[12:15], v[132:135], v[212:215], v[12:15]
	v_mfma_f32_16x16x32_bf16 v[8:11], v[140:143], v[212:215], v[8:11]
	s_setprio 0
	s_cmp_eq_u32 s14, 8
	s_cbranch_scc1 .Lmy_p2skip2
	s_setprio 1
	v_mfma_f32_16x16x32_bf16 v[52:55], v[144:147], v[182:185], v[52:55]
	v_mfma_f32_16x16x32_bf16 v[48:51], v[166:169], v[182:185], v[48:51]
	v_mfma_f32_16x16x32_bf16 v[36:39], v[144:147], v[190:193], v[36:39]
	v_mfma_f32_16x16x32_bf16 v[32:35], v[166:169], v[190:193], v[32:35]
	v_mfma_f32_16x16x32_bf16 v[20:23], v[144:147], v[200:203], v[20:23]
	v_mfma_f32_16x16x32_bf16 v[16:19], v[166:169], v[200:203], v[16:19]
	v_mfma_f32_16x16x32_bf16 v[4:7], v[144:147], v[208:211], v[4:7]
	v_mfma_f32_16x16x32_bf16 v[0:3], v[166:169], v[208:211], v[0:3]
	v_mfma_f32_16x16x32_bf16 v[52:55], v[148:151], v[186:189], v[52:55]
	v_mfma_f32_16x16x32_bf16 v[48:51], v[170:173], v[186:189], v[48:51]
	v_mfma_f32_16x16x32_bf16 v[36:39], v[148:151], v[194:197], v[36:39]
	v_mfma_f32_16x16x32_bf16 v[32:35], v[170:173], v[194:197], v[32:35]
	v_mfma_f32_16x16x32_bf16 v[20:23], v[148:151], v[204:207], v[20:23]
	v_mfma_f32_16x16x32_bf16 v[16:19], v[170:173], v[204:207], v[16:19]
	v_mfma_f32_16x16x32_bf16 v[4:7], v[148:151], v[212:215], v[4:7]
	v_mfma_f32_16x16x32_bf16 v[0:3], v[170:173], v[212:215], v[0:3]
.Lmy_p2skip2:
	s_setprio 0
	s_barrier
	s_add_i32 vcc_lo, 0, 0x18000
	s_add_i32 vcc_hi, 0, 0x1c000
	v_add_u32_e32 v140, vcc_lo, v174
	v_add_u32_e32 v160, vcc_hi, v174
	ds_read_b128 v[128:131], v140
	ds_read_b128 v[132:135], v140 offset:1024
	ds_read_b128 v[136:139], v140 offset:2048
	ds_read_b128 v[140:143], v140 offset:3072
	ds_read_b128 v[144:147], v160
	ds_read_b128 v[148:151], v160 offset:1024
	ds_read_b128 v[166:169], v160 offset:2048
	ds_read_b128 v[170:173], v160 offset:3072
	s_add_u32 s96, s60, 0x40000
	s_addc_u32 s97, s61, 0
	s_mov_b32 m0, s75
	ds_read_b128 v[182:185], v177 offset:32768
	ds_read_b128 v[186:189], v177 offset:33792
	ds_read_b128 v[190:193], v177 offset:34816
	ds_read_b128 v[194:197], v177 offset:35840
	ds_read_b128 v[200:203], v177 offset:36864
	ds_read_b128 v[204:207], v177 offset:37888
	ds_read_b128 v[208:211], v177 offset:38912
	ds_read_b128 v[212:215], v177 offset:39936
	global_load_lds_dwordx4 v152, s[96:97]
	s_mov_b32 m0, s76
	s_nop 0
	global_load_lds_dwordx4 v156, s[96:97]
	s_cmp_lg_u32 s95, 0
	s_cbranch_scc1 .Lwvr2
	s_waitcnt vmcnt(8)

; #define PG8_STAGE(bufoff, gbase, voff) do { _Pragma("unroll") for (int _i = 0; _i < 2; ++_i) \
;         __builtin_amdgcn_global_load_lds((const unsigned*)((const char*)(gbase) + (voff)[_i]), (LAS unsigned*)(lds + (bufoff) + ldsw + _i * 8192), 16, 0, 0); } while (0)
; #define PG8_LDA(dst, b, h) do { _Pragma("unroll") for (int m = 0; m < 4; ++m) _Pragma("unroll") for (int k = 0; k < 2; ++k) dst[m][k] = *(const LAS bf16x8*)(lds + PG8_SA(b, h) + aoff + m * 2048 + k * 1024); } while (0)
; #define PG8_LDB(dst, b, h) do { _Pragma("unroll") for (int n = 0; n < 2; ++n) _Pragma("unroll") for (int k = 0; k < 2; ++k) dst[n][k] = *(const LAS bf16x8*)(lds + PG8_SB(b, h) + boff + n * 2048 + k * 1024); } while (0)
; #define PG8_MMA(ai, bj, At, Bt_) do { __builtin_amdgcn_s_setprio(1); _Pragma("unroll") for (int m = 0; m < 4; ++m) _Pragma("unroll") for (int n = 0; n < 2; ++n) _Pragma("unroll") for (int k = 0; k < 2; ++k) \
;         acc[ai][bj][m][n] = __builtin_amdgcn_mfma_f32_16x16x32_bf16(Bt_[n][k], At[m][k], acc[ai][bj][m][n], 0, 0, 0); __builtin_amdgcn_s_setprio(0); } while (0)
; #define PG8_WAIT_V(n) asm volatile("s_waitcnt vmcnt(" #n ")" ::: "memory")
; #define PG8_WAIT_L(n) asm volatile("s_waitcnt lgkmcnt(" #n ")" ::: "memory")
; #define PG8_WAIT_VR(rl) asm volatile("s_cmp_lg_u32 %0, 0\n\ts_cbranch_scc1 .Lwvr%=\n\ts_waitcnt vmcnt(8)\n.Lwvr%=:\n\ts_waitcnt vmcnt(24)" :: "s"(rl) : "scc", "memory")
; #define PG8_BAR __builtin_amdgcn_s_barrier()
; #define PG8_SCHED __builtin_amdgcn_sched_barrier(0)
; template <class Epi, class Sched, bool GATHER>
; __device__ __forceinline__ void gemm_phase(LAS unsigned char* lds, const int wid, const bf16_t* A, int lda, const bf16_t* Bt, int ldb, size_t b_estride, int K, const Sched& S, const Epi& E) {
;     ...
;             PG8_LDB(B0, 1, 0); PG8_LDB(B1, 1, 1); PG8_SCHED; PG8_LDA(At, 1, 0); PG8_STAGE_A(PG8_SA(0, 1), a2, 1, k2, g21);
;             PG8_WAIT_VR(rl); PG8_WAIT_L(0); PG8_BAR; PG8_MMA(0, 0, At, B0); PG8_MMA(0, 1, At, B1); PG8_BAR; PG8_SCHED;
;             PG8_LDA(At, 1, 1); PG8_STAGE(PG8_SB(1, 0), b3, voffB); PG8_STAGE(PG8_SB(1, 1), b3 + hstepB, voffB); PG8_STAGE_A(PG8_SA(1, 0), a3, 0, k3, g20);
;             PG8_WAIT_V(8); PG8_WAIT_L(0); PG8_BAR; PG8_MMA(1, 0, At, B0); PG8_MMA(1, 1, At, B1); PG8_BAR; PG8_SCHED;
;             PG8_STAGE_A(PG8_SA(1, 1), a3, 1, k3, g21);
;         }
.Lmy_p2skip3:
	s_setprio 0
	s_barrier
	s_add_i32 s95, vcc_lo, s33
	s_mov_b32 m0, s95
	ds_read_b128 v[182:185], v177 offset:49152
	ds_read_b128 v[186:189], v177 offset:50176
	ds_read_b128 v[190:193], v177 offset:51200
	ds_read_b128 v[194:197], v177 offset:52224
	ds_read_b128 v[200:203], v177 offset:53248
	ds_read_b128 v[204:207], v177 offset:54272
	ds_read_b128 v[208:211], v177 offset:55296
	ds_read_b128 v[212:215], v177 offset:56320
	global_load_lds_dwordx4 v154, s[98:99]
	s_add_i32 m0, s95, 0x2000
	s_add_u32 s70, s70, 0x40080
	s_addc_u32 s71, s71, 0
	s_add_i32 s95, vcc_hi, s33
	global_load_lds_dwordx4 v158, s[98:99]
	s_mov_b32 m0, s95
	s_nop 0
	global_load_lds_dwordx4 v154, s[70:71]
	s_add_i32 m0, s95, 0x2000
	s_nop 0
	global_load_lds_dwordx4 v158, s[70:71]
	s_mov_b32 m0, s81
	s_nop 0
	global_load_lds_dwordx4 v152, s[100:101]
	s_mov_b32 m0, s82
	s_nop 0
	global_load_lds_dwordx4 v156, s[100:101]
	s_waitcnt vmcnt(8)
	s_waitcnt lgkmcnt(0)
	s_barrier
	s_setprio 1
	s_waitcnt lgkmcnt(0)
	v_mfma_f32_16x16x32_bf16 v[60:63], v[128:131], v[182:185], v[60:63]
	v_mfma_f32_16x16x32_bf16 v[56:59], v[136:139], v[182:185], v[56:59]
	v_mfma_f32_16x16x32_bf16 v[44:47], v[128:131], v[190:193], v[44:47]
	v_mfma_f32_16x16x32_bf16 v[40:43], v[136:139], v[190:193], v[40:43]
	v_mfma_f32_16x16x32_bf16 v[28:31], v[128:131], v[200:203], v[28:31]
	v_mfma_f32_16x16x32_bf16 v[24:27], v[136:139], v[200:203], v[24:27]
	v_mfma_f32_16x16x32_bf16 v[12:15], v[128:131], v[208:211], v[12:15]
	v_mfma_f32_16x16x32_bf16 v[8:11], v[136:139], v[208:211], v[8:11]
	v_mfma_f32_16x16x32_bf16 v[60:63], v[132:135], v[186:189], v[60:63]
	v_mfma_f32_16x16x32_bf16 v[56:59], v[140:143], v[186:189], v[56:59]
	v_mfma_f32_16x16x32_bf16 v[44:47], v[132:135], v[194:197], v[44:47]
	v_mfma_f32_16x16x32_bf16 v[40:43], v[140:143], v[194:197], v[40:43]
	v_mfma_f32_16x16x32_bf16 v[28:31], v[132:135], v[204:207], v[28:31]
	v_mfma_f32_16x16x32_bf16 v[24:27], v[140:143], v[204:207], v[24:27]
	v_mfma_f32_16x16x32_bf16 v[12:15], v[132:135], v[212:215], v[12:15]
	v_mfma_f32_16x16x32_bf16 v[8:11], v[140:143], v[212:215], v[8:11]
	s_setprio 0
	s_cmp_eq_u32 s14, 8
	s_cbranch_scc1 .Lmy_p2skip4
	s_setprio 1
	v_mfma_f32_16x16x32_bf16 v[52:55], v[144:147], v[182:185], v[52:55]
	v_mfma_f32_16x16x32_bf16 v[48:51], v[166:169], v[182:185], v[48:51]
	v_mfma_f32_16x16x32_bf16 v[36:39], v[144:147], v[190:193], v[36:39]
	v_mfma_f32_16x16x32_bf16 v[32:35], v[166:169], v[190:193], v[32:35]
	v_mfma_f32_16x16x32_bf16 v[20:23], v[144:147], v[200:203], v[20:23]
	v_mfma_f32_16x16x32_bf16 v[16:19], v[166:169], v[200:203], v[16:19]
	v_mfma_f32_16x16x32_bf16 v[4:7], v[144:147], v[208:211], v[4:7]
	v_mfma_f32_16x16x32_bf16 v[0:3], v[166:169], v[208:211], v[0:3]
	v_mfma_f32_16x16x32_bf16 v[52:55], v[148:151], v[186:189], v[52:55]
	v_mfma_f32_16x16x32_bf16 v[48:51], v[170:173], v[186:189], v[48:51]
	v_mfma_f32_16x16x32_bf16 v[36:39], v[148:151], v[194:197], v[36:39]
	v_mfma_f32_16x16x32_bf16 v[32:35], v[170:173], v[194:197], v[32:35]
	v_mfma_f32_16x16x32_bf16 v[20:23], v[148:151], v[204:207], v[20:23]
	v_mfma_f32_16x16x32_bf16 v[16:19], v[170:173], v[204:207], v[16:19]
	v_mfma_f32_16x16x32_bf16 v[4:7], v[148:151], v[212:215], v[4:7]
	v_mfma_f32_16x16x32_bf16 v[0:3], v[170:173], v[212:215], v[0:3]
.Lmy_p2skip4:
	s_setprio 0
	s_barrier
	s_add_u32 s60, s60, 0x40080
	s_addc_u32 s61, s61, 0
	s_mov_b32 m0, s83
	s_nop 0
	global_load_lds_dwordx4 v152, s[60:61]
	s_mov_b32 m0, s84
	s_add_i32 s94, s94, 2
	global_load_lds_dwordx4 v156, s[60:61]
	s_add_u32 s52, s52, 0x100
	s_addc_u32 s53, s53, 0
	s_add_u32 s92, s92, 0x100
	s_addc_u32 s93, s93, 0
	s_cmp_gt_u32 s94, 13
	s_cbranch_scc0 .LBB0_268
	s_and_b64 vcc, exec, s[40:41]
	s_cbranch_vccz .LBB0_271
	s_barrier
